# best version with a 4-byte code shift at main kernel entry (code placement check)
# speedup vs baseline: 1.0100x; 1.0074x over previous
_Z11main_kernelPKfS0_PKDF16_S0_PfS3_:
	s_nop 0
	s_load_dwordx4 s[16:19], s[0:1], 0x0
	s_load_dwordx2 s[14:15], s[0:1], 0x28
	v_readfirstlane_b32 s3, v0
	v_and_b32_e32 v164, 63, v0
	s_ashr_i32 s33, s3, 6
	v_lshlrev_b32_e32 v162, 4, v164
	s_cmp_lg_u32 s33, 4
	s_mov_b64 s[4:5], -1
	s_cbranch_scc0 .LBB1_183
	s_load_dwordx2 s[20:21], s[0:1], 0x20
	s_lshl_b32 s98, s2, 7
	s_add_i32 s23, s33, -5
	s_cmp_gt_u32 s23, 1
	s_cbranch_scc0 .LBB1_142
	s_cmp_lg_u32 s33, 7
	v_writelane_b32 v216, s23, 0
	s_cbranch_scc0 .LBB1_95
	s_lshl_b32 s3, s33, 5
	s_add_i32 s10, s3, s98
	s_or_b32 s4, s10, 1
	s_ashr_i32 s5, s4, 31
	s_lshl_b64 s[8:9], s[4:5], 10
	s_or_b32 s4, s10, 2
	s_ashr_i32 s5, s4, 31
	s_lshl_b64 s[12:13], s[4:5], 10
	s_or_b32 s4, s10, 3
	s_ashr_i32 s5, s4, 31
	s_lshl_b64 s[22:23], s[4:5], 10
	s_or_b32 s4, s10, 4
	s_ashr_i32 s5, s4, 31
	s_lshl_b64 s[24:25], s[4:5], 10
	s_or_b32 s4, s10, 5
	s_ashr_i32 s5, s4, 31
	s_lshl_b64 s[28:29], s[4:5], 10
	s_or_b32 s4, s10, 6
	s_ashr_i32 s5, s4, 31
	s_lshl_b64 s[26:27], s[4:5], 10
	s_or_b32 s4, s10, 7
	s_ashr_i32 s5, s4, 31
	s_lshl_b64 s[30:31], s[4:5], 10
	s_or_b32 s4, s10, 8
	s_ashr_i32 s5, s4, 31
	s_lshl_b64 s[34:35], s[4:5], 10
	s_or_b32 s4, s10, 9
	s_ashr_i32 s5, s4, 31
	s_lshl_b64 s[38:39], s[4:5], 10
	s_or_b32 s4, s10, 10
	s_ashr_i32 s5, s4, 31
	s_lshl_b64 s[36:37], s[4:5], 10
	s_or_b32 s4, s10, 11
	s_ashr_i32 s5, s4, 31
	s_lshl_b64 s[40:41], s[4:5], 10
	s_or_b32 s4, s10, 12
	s_ashr_i32 s5, s4, 31
	s_lshl_b64 s[42:43], s[4:5], 10
	s_or_b32 s4, s10, 13
	s_ashr_i32 s5, s4, 31
	s_lshl_b64 s[46:47], s[4:5], 10
	s_or_b32 s4, s10, 14
	v_mov_b32_e32 v163, 0
	s_ashr_i32 s11, s10, 31
	s_ashr_i32 s5, s4, 31
	s_waitcnt lgkmcnt(0)
	v_lshl_add_u64 v[166:167], s[16:17], 0, v[162:163]
	s_lshl_b64 s[6:7], s[10:11], 10
	s_lshl_b64 s[44:45], s[4:5], 10
	s_mul_i32 s4, s33, 0x4200
	v_lshl_add_u64 v[2:3], v[166:167], 0, s[6:7]
	v_mov_b32_e32 v1, s4
	v_lshl_or_b32 v78, v164, 3, s4
	s_or_b32 s4, s10, 15
	v_lshl_add_u64 v[4:5], v[166:167], 0, s[8:9]
	global_load_dwordx4 v[6:9], v[2:3], off nt
	global_load_dwordx4 v[10:13], v[4:5], off nt
	s_ashr_i32 s5, s4, 31
	v_lshl_add_u64 v[2:3], v[166:167], 0, s[12:13]
	s_lshl_b64 s[4:5], s[4:5], 10
	v_lshl_add_u64 v[4:5], v[166:167], 0, s[22:23]
	global_load_dwordx4 v[14:17], v[2:3], off nt
	global_load_dwordx4 v[18:21], v[4:5], off nt
	v_lshl_add_u64 v[2:3], v[166:167], 0, s[24:25]
	v_lshl_add_u64 v[66:67], v[166:167], 0, s[4:5]
	global_load_dwordx4 v[22:25], v[2:3], off nt
	v_add_u32_e32 v79, 0x1800, v78
	global_load_dwordx4 v[66:69], v[66:67], off nt
	v_lshl_add_u64 v[2:3], v[166:167], 0, s[28:29]
	global_load_dwordx4 v[26:29], v[2:3], off nt
	v_lshl_add_u64 v[2:3], v[166:167], 0, s[26:27]
	global_load_dwordx4 v[30:33], v[2:3], off nt
	v_lshl_add_u64 v[2:3], v[166:167], 0, s[30:31]
	global_load_dwordx4 v[34:37], v[2:3], off nt
	v_lshl_add_u64 v[2:3], v[166:167], 0, s[34:35]
	global_load_dwordx4 v[38:41], v[2:3], off nt
	v_lshl_add_u64 v[2:3], v[166:167], 0, s[38:39]
	global_load_dwordx4 v[42:45], v[2:3], off nt
	v_lshl_add_u64 v[2:3], v[166:167], 0, s[36:37]
	global_load_dwordx4 v[46:49], v[2:3], off nt
	v_lshl_add_u64 v[2:3], v[166:167], 0, s[40:41]
	global_load_dwordx4 v[50:53], v[2:3], off nt
	v_lshl_add_u64 v[2:3], v[166:167], 0, s[42:43]
	global_load_dwordx4 v[54:57], v[2:3], off nt
	v_lshl_add_u64 v[2:3], v[166:167], 0, s[46:47]
	global_load_dwordx4 v[58:61], v[2:3], off nt
	v_lshl_add_u64 v[2:3], v[166:167], 0, s[44:45]
	global_load_dwordx4 v[62:65], v[2:3], off nt
	v_lshl_add_u64 v[2:3], s[20:21], 0, v[162:163]
	v_lshl_add_u64 v[70:71], v[2:3], 0, s[6:7]
	s_or_b32 s6, s10, 16
	s_ashr_i32 s7, s6, 31
	s_lshl_b64 s[6:7], s[6:7], 10
	s_or_b32 s48, s10, 31
	s_ashr_i32 s49, s48, 31
	s_lshl_b64 s[48:49], s[48:49], 10
	v_lshl_add_u64 v[74:75], v[166:167], 0, s[48:49]
	v_and_b32_e32 v4, 31, v0
	v_lshrrev_b32_e32 v5, 5, v164
	v_add_u32_e32 v182, s10, v164
	v_mov_b32_e32 v179, 0x260
	v_add_u32_e32 v185, s3, v164
	v_mov_b32_e32 v177, 0xfffffe00
	v_or_b32_e32 v181, 0x10800, v162
	v_lshlrev_b32_e32 v184, 2, v5
	v_lshl_or_b32 v189, s33, 13, v164
	v_mov_b32_e32 v190, 0x22630
	v_mov_b32_e32 v191, 0x22634
	v_mov_b32_e32 v192, 0x22610
	v_mov_b32_e32 v193, 0x22600
	s_mov_b32 s50, 0x22624
	v_mov_b32_e32 v194, 0x22400
	v_mov_b32_e32 v170, 0x8800759c
	v_mov_b32_e32 v171, 0x7e37e43c
	s_waitcnt vmcnt(15)
	global_store_dwordx4 v[70:71], v[6:9], off nt
	s_nop 1
	v_cvt_pk_f16_f32 v9, v8, v9
	v_cvt_pk_f16_f32 v8, v6, v7
	v_lshl_add_u64 v[6:7], v[2:3], 0, s[8:9]
	s_waitcnt vmcnt(15)
	global_store_dwordx4 v[6:7], v[10:13], off nt
	v_cvt_pk_f16_f32 v7, v12, v13
	v_cvt_pk_f16_f32 v6, v10, v11
	ds_write2_b64 v78, v[8:9], v[6:7] offset1:66
	v_lshl_add_u64 v[6:7], v[2:3], 0, s[12:13]
	v_lshl_add_u64 v[8:9], v[2:3], 0, s[22:23]
	s_waitcnt vmcnt(15)
	global_store_dwordx4 v[6:7], v[14:17], off nt
	v_cvt_pk_f16_f32 v7, v16, v17
	v_cvt_pk_f16_f32 v6, v14, v15
	s_waitcnt vmcnt(15)
	global_store_dwordx4 v[8:9], v[18:21], off nt
	v_cvt_pk_f16_f32 v9, v20, v21
	v_cvt_pk_f16_f32 v8, v18, v19
	ds_write2_b64 v78, v[6:7], v[8:9] offset0:132 offset1:198
	v_lshl_add_u64 v[6:7], v[2:3], 0, s[24:25]
	v_lshl_add_u64 v[8:9], v[2:3], 0, s[28:29]
	s_waitcnt vmcnt(15)
	global_store_dwordx4 v[6:7], v[22:25], off nt
	v_cvt_pk_f16_f32 v7, v24, v25
	v_cvt_pk_f16_f32 v6, v22, v23
	s_waitcnt vmcnt(14)
	global_store_dwordx4 v[8:9], v[26:29], off nt
	v_cvt_pk_f16_f32 v9, v28, v29
	v_cvt_pk_f16_f32 v8, v26, v27
	v_add_u32_e32 v10, 0x800, v78
	ds_write2_b64 v10, v[6:7], v[8:9] offset0:8 offset1:74
	v_lshl_add_u64 v[6:7], v[2:3], 0, s[26:27]
	v_lshl_add_u64 v[8:9], v[2:3], 0, s[30:31]
	s_waitcnt vmcnt(14)
	global_store_dwordx4 v[6:7], v[30:33], off nt
	v_cvt_pk_f16_f32 v7, v32, v33
	v_cvt_pk_f16_f32 v6, v30, v31
	s_waitcnt vmcnt(14)
	global_store_dwordx4 v[8:9], v[34:37], off nt
	v_cvt_pk_f16_f32 v9, v36, v37
	v_cvt_pk_f16_f32 v8, v34, v35
	ds_write2_b64 v10, v[6:7], v[8:9] offset0:140 offset1:206
	v_lshl_add_u64 v[6:7], v[2:3], 0, s[34:35]
	v_lshl_add_u64 v[8:9], v[2:3], 0, s[38:39]
	s_waitcnt vmcnt(14)
	global_store_dwordx4 v[6:7], v[38:41], off nt
	v_cvt_pk_f16_f32 v7, v40, v41
	v_cvt_pk_f16_f32 v6, v38, v39
	s_waitcnt vmcnt(14)
	global_store_dwordx4 v[8:9], v[42:45], off nt
	v_cvt_pk_f16_f32 v9, v44, v45
	v_cvt_pk_f16_f32 v8, v42, v43
	v_add_u32_e32 v10, 0x1000, v78
	ds_write2_b64 v10, v[6:7], v[8:9] offset0:16 offset1:82
	v_lshl_add_u64 v[6:7], v[2:3], 0, s[36:37]
	v_lshl_add_u64 v[8:9], v[2:3], 0, s[40:41]
	s_waitcnt vmcnt(14)
	global_store_dwordx4 v[6:7], v[46:49], off nt
	v_cvt_pk_f16_f32 v7, v48, v49
	v_cvt_pk_f16_f32 v6, v46, v47
	s_waitcnt vmcnt(14)
	global_store_dwordx4 v[8:9], v[50:53], off nt
	v_cvt_pk_f16_f32 v9, v52, v53
	v_cvt_pk_f16_f32 v8, v50, v51
	ds_write2_b64 v10, v[6:7], v[8:9] offset0:148 offset1:214
	v_lshl_add_u64 v[6:7], v[2:3], 0, s[42:43]
	v_lshl_add_u64 v[8:9], v[2:3], 0, s[46:47]
	s_waitcnt vmcnt(14)
	global_store_dwordx4 v[6:7], v[54:57], off nt
	v_cvt_pk_f16_f32 v7, v56, v57
	v_cvt_pk_f16_f32 v6, v54, v55
	s_waitcnt vmcnt(14)
	global_store_dwordx4 v[8:9], v[58:61], off nt
	v_cvt_pk_f16_f32 v9, v60, v61
	v_cvt_pk_f16_f32 v8, v58, v59
	s_or_b32 s8, s10, 17
	ds_write2_b64 v79, v[6:7], v[8:9] offset0:24 offset1:90
	v_lshl_add_u64 v[6:7], v[2:3], 0, s[44:45]
	s_ashr_i32 s9, s8, 31
	s_or_b32 s12, s10, 18
	s_waitcnt vmcnt(14)
	global_store_dwordx4 v[6:7], v[62:65], off nt
	v_lshl_add_u64 v[14:15], v[166:167], 0, s[6:7]
	s_lshl_b64 s[8:9], s[8:9], 10
	s_ashr_i32 s13, s12, 31
	s_or_b32 s22, s10, 19
	v_lshl_add_u64 v[16:17], v[166:167], 0, s[8:9]
	global_load_dwordx4 v[6:9], v[14:15], off nt
	global_load_dwordx4 v[10:13], v[16:17], off nt
	s_lshl_b64 s[12:13], s[12:13], 10
	s_ashr_i32 s23, s22, 31
	s_or_b32 s24, s10, 20
	s_or_b32 s26, s10, 21
	v_lshl_add_u64 v[22:23], v[166:167], 0, s[12:13]
	s_lshl_b64 s[22:23], s[22:23], 10
	s_ashr_i32 s25, s24, 31
	s_ashr_i32 s27, s26, 31
	v_lshl_add_u64 v[24:25], v[166:167], 0, s[22:23]
	global_load_dwordx4 v[14:17], v[22:23], off nt
	global_load_dwordx4 v[18:21], v[24:25], off nt
	s_lshl_b64 s[24:25], s[24:25], 10
	s_lshl_b64 s[28:29], s[26:27], 10
	s_or_b32 s26, s10, 22
	s_or_b32 s30, s10, 23
	v_lshl_add_u64 v[22:23], v[166:167], 0, s[24:25]
	v_lshl_add_u64 v[26:27], v[166:167], 0, s[28:29]
	s_ashr_i32 s27, s26, 31
	s_ashr_i32 s31, s30, 31
	global_load_dwordx4 v[22:25], v[22:23], off nt
	s_lshl_b64 s[26:27], s[26:27], 10
	global_load_dwordx4 v[26:29], v[26:27], off nt
	s_lshl_b64 s[30:31], s[30:31], 10
	s_or_b32 s34, s10, 24
	s_or_b32 s36, s10, 25
	v_lshl_add_u64 v[30:31], v[166:167], 0, s[26:27]
	v_lshl_add_u64 v[34:35], v[166:167], 0, s[30:31]
	s_ashr_i32 s35, s34, 31
	s_ashr_i32 s37, s36, 31
	global_load_dwordx4 v[30:33], v[30:31], off nt
	s_lshl_b64 s[34:35], s[34:35], 10
	global_load_dwordx4 v[34:37], v[34:35], off nt
	s_lshl_b64 s[38:39], s[36:37], 10
	s_or_b32 s36, s10, 26
	s_or_b32 s40, s10, 27
	v_lshl_add_u64 v[38:39], v[166:167], 0, s[34:35]
	v_lshl_add_u64 v[42:43], v[166:167], 0, s[38:39]
	s_ashr_i32 s37, s36, 31
	s_ashr_i32 s41, s40, 31
	global_load_dwordx4 v[38:41], v[38:39], off nt
	s_lshl_b64 s[36:37], s[36:37], 10
	global_load_dwordx4 v[42:45], v[42:43], off nt
	s_lshl_b64 s[40:41], s[40:41], 10
	s_or_b32 s42, s10, 28
	s_or_b32 s44, s10, 29
	v_lshl_add_u64 v[46:47], v[166:167], 0, s[36:37]
	v_lshl_add_u64 v[50:51], v[166:167], 0, s[40:41]
	s_ashr_i32 s43, s42, 31
	s_ashr_i32 s45, s44, 31
	global_load_dwordx4 v[46:49], v[46:47], off nt
	s_lshl_b64 s[42:43], s[42:43], 10
	global_load_dwordx4 v[50:53], v[50:51], off nt
	s_lshl_b64 s[46:47], s[44:45], 10
	s_or_b32 s44, s10, 30
	v_lshl_add_u64 v[54:55], v[166:167], 0, s[42:43]
	v_lshl_add_u64 v[58:59], v[166:167], 0, s[46:47]
	s_ashr_i32 s45, s44, 31
	global_load_dwordx4 v[54:57], v[54:55], off nt
	s_lshl_b64 s[44:45], s[44:45], 10
	global_load_dwordx4 v[58:61], v[58:59], off nt
	v_lshl_add_u64 v[70:71], v[166:167], 0, s[44:45]
	global_load_dwordx4 v[70:73], v[70:71], off nt
	v_cvt_pk_f16_f32 v65, v64, v65
	global_load_dwordx4 v[74:77], v[74:75], off nt
	v_cvt_pk_f16_f32 v64, v62, v63
	v_lshl_add_u64 v[62:63], v[2:3], 0, s[4:5]
	global_store_dwordx4 v[62:63], v[66:69], off nt
	v_cvt_pk_f16_f32 v63, v68, v69
	v_cvt_pk_f16_f32 v62, v66, v67
	ds_write2_b64 v79, v[64:65], v[62:63] offset0:156 offset1:222
	v_lshl_add_u64 v[62:63], v[2:3], 0, s[6:7]
	s_movk_i32 s4, 0x210
	v_mad_u32_u24 v1, v4, s4, v1
	s_add_i32 s10, s10, 0x18000
	s_ashr_i32 s11, s10, 31
	v_add_u32_e32 v187, s10, v164
	s_lshl_b64 s[10:11], s[10:11], 10
	v_cmp_eq_u32_e64 s[6:7], 0, v164
	s_waitcnt vmcnt(16)
	global_store_dwordx4 v[62:63], v[6:9], off nt
	s_nop 1
	v_cvt_pk_f16_f32 v9, v8, v9
	v_cvt_pk_f16_f32 v8, v6, v7
	v_lshl_add_u64 v[6:7], v[2:3], 0, s[8:9]
	s_waitcnt vmcnt(16)
	global_store_dwordx4 v[6:7], v[10:13], off nt
	v_cvt_pk_f16_f32 v7, v12, v13
	v_cvt_pk_f16_f32 v6, v10, v11
	v_add_u32_e32 v10, 0x2000, v78
	ds_write2_b64 v10, v[8:9], v[6:7] offset0:32 offset1:98
	v_lshl_add_u64 v[6:7], v[2:3], 0, s[12:13]
	v_lshl_add_u64 v[8:9], v[2:3], 0, s[22:23]
	s_waitcnt vmcnt(16)
	global_store_dwordx4 v[6:7], v[14:17], off nt
	v_cvt_pk_f16_f32 v7, v16, v17
	v_cvt_pk_f16_f32 v6, v14, v15
	s_waitcnt vmcnt(16)
	global_store_dwordx4 v[8:9], v[18:21], off nt
	v_cvt_pk_f16_f32 v9, v20, v21
	v_cvt_pk_f16_f32 v8, v18, v19
	ds_write2_b64 v10, v[6:7], v[8:9] offset0:164 offset1:230
	v_lshl_add_u64 v[6:7], v[2:3], 0, s[24:25]
	v_lshl_add_u64 v[8:9], v[2:3], 0, s[28:29]
	s_waitcnt vmcnt(16)
	global_store_dwordx4 v[6:7], v[22:25], off nt
	v_cvt_pk_f16_f32 v7, v24, v25
	v_cvt_pk_f16_f32 v6, v22, v23
	s_waitcnt vmcnt(16)
	global_store_dwordx4 v[8:9], v[26:29], off nt
	v_cvt_pk_f16_f32 v9, v28, v29
	v_cvt_pk_f16_f32 v8, v26, v27
	v_add_u32_e32 v10, 0x2800, v78
	ds_write2_b64 v10, v[6:7], v[8:9] offset0:40 offset1:106
	v_lshl_add_u64 v[6:7], v[2:3], 0, s[26:27]
	v_lshl_add_u64 v[8:9], v[2:3], 0, s[30:31]
	s_waitcnt vmcnt(16)
	global_store_dwordx4 v[6:7], v[30:33], off nt
	v_cvt_pk_f16_f32 v7, v32, v33
	v_cvt_pk_f16_f32 v6, v30, v31
	s_waitcnt vmcnt(16)
	global_store_dwordx4 v[8:9], v[34:37], off nt
	v_cvt_pk_f16_f32 v9, v36, v37
	v_cvt_pk_f16_f32 v8, v34, v35
	ds_write2_b64 v10, v[6:7], v[8:9] offset0:172 offset1:238
	v_lshl_add_u64 v[6:7], v[2:3], 0, s[34:35]
	v_lshl_add_u64 v[8:9], v[2:3], 0, s[38:39]
	s_waitcnt vmcnt(16)
	global_store_dwordx4 v[6:7], v[38:41], off nt
	v_cvt_pk_f16_f32 v7, v40, v41
	v_cvt_pk_f16_f32 v6, v38, v39
	s_waitcnt vmcnt(16)
	global_store_dwordx4 v[8:9], v[42:45], off nt
	v_cvt_pk_f16_f32 v9, v44, v45
	v_cvt_pk_f16_f32 v8, v42, v43
	v_add_u32_e32 v10, 0x3000, v78
	ds_write2_b64 v10, v[6:7], v[8:9] offset0:48 offset1:114
	v_lshl_add_u64 v[6:7], v[2:3], 0, s[36:37]
	v_lshl_add_u64 v[8:9], v[2:3], 0, s[40:41]
	s_waitcnt vmcnt(16)
	global_store_dwordx4 v[6:7], v[46:49], off nt
	v_cvt_pk_f16_f32 v7, v48, v49
	v_cvt_pk_f16_f32 v6, v46, v47
	s_waitcnt vmcnt(16)
	global_store_dwordx4 v[8:9], v[50:53], off nt
	v_cvt_pk_f16_f32 v9, v52, v53
	v_cvt_pk_f16_f32 v8, v50, v51
	ds_write2_b64 v10, v[6:7], v[8:9] offset0:180 offset1:246
	v_lshl_add_u64 v[6:7], v[2:3], 0, s[42:43]
	v_lshl_add_u64 v[8:9], v[2:3], 0, s[46:47]
	s_waitcnt vmcnt(16)
	global_store_dwordx4 v[6:7], v[54:57], off nt
	v_cvt_pk_f16_f32 v7, v56, v57
	v_cvt_pk_f16_f32 v6, v54, v55
	s_waitcnt vmcnt(16)
	global_store_dwordx4 v[8:9], v[58:61], off nt
	v_cvt_pk_f16_f32 v9, v60, v61
	v_cvt_pk_f16_f32 v8, v58, v59
	v_add_u32_e32 v10, 0x3800, v78
	ds_write2_b64 v10, v[6:7], v[8:9] offset0:56 offset1:122
	v_lshl_add_u64 v[6:7], v[2:3], 0, s[44:45]
	v_lshl_add_u64 v[2:3], v[2:3], 0, s[48:49]
	s_waitcnt vmcnt(16)
	global_store_dwordx4 v[6:7], v[70:73], off nt
	v_cvt_pk_f16_f32 v7, v72, v73
	v_cvt_pk_f16_f32 v6, v70, v71
	s_waitcnt vmcnt(16)
	global_store_dwordx4 v[2:3], v[74:77], off nt
	v_cvt_pk_f16_f32 v3, v76, v77
	v_cvt_pk_f16_f32 v2, v74, v75
	ds_write2_b64 v10, v[6:7], v[2:3] offset0:188 offset1:254
	v_lshlrev_b32_e32 v2, 4, v5
	v_add_u32_e32 v176, v1, v2
	v_mbcnt_lo_u32_b32 v1, -1, 0
	v_mbcnt_hi_u32_b32 v14, -1, v1
	v_and_b32_e32 v6, 64, v14
	v_lshlrev_b32_e32 v10, 5, v164
	v_add_u32_e32 v15, 64, v6
	v_or_b32_e32 v6, 0x20800, v10
	s_waitcnt lgkmcnt(0)
	s_barrier
	ds_read_b128 v[94:97], v176
	ds_read_b128 v[90:93], v176 offset:32
	ds_read_b128 v[86:89], v176 offset:64
	ds_read_b128 v[82:85], v176 offset:96
	ds_read_b128 v[78:81], v176 offset:128
	ds_read_b128 v[74:77], v176 offset:160
	ds_read_b128 v[70:73], v176 offset:192
	ds_read_b128 v[66:69], v176 offset:224
	ds_read_b128 v[62:65], v176 offset:256
	ds_read_b128 v[58:61], v176 offset:288
	ds_read_b128 v[54:57], v176 offset:320
	ds_read_b128 v[50:53], v176 offset:352
	ds_read_b128 v[46:49], v176 offset:384
	ds_read_b128 v[42:45], v176 offset:416
	ds_read_b128 v[38:41], v176 offset:448
	ds_read_b128 v[34:37], v176 offset:480
	ds_read_b128 v[6:9], v6
	v_or_b32_e32 v10, 0x20810, v10
	ds_read_b128 v[10:13], v10
	v_mov_b32_e32 v3, v163
	s_waitcnt lgkmcnt(14)
	v_dot2c_f32_f16_e32 v3, v94, v94
	s_waitcnt lgkmcnt(1)
	v_max_f32_e32 v7, v7, v7
	v_max_f32_e32 v6, v6, v6
	v_max_f32_e32 v6, v6, v7
	v_max_f32_e32 v7, v9, v9
	v_max_f32_e32 v8, v8, v8
	v_dot2c_f32_f16_e32 v3, v95, v95
	v_xor_b32_e32 v1, 32, v14
	v_max_f32_e32 v7, v8, v7
	s_waitcnt lgkmcnt(0)
	v_max_f32_e32 v8, v13, v13
	v_max_f32_e32 v9, v12, v12
	v_dot2c_f32_f16_e32 v3, v96, v96
	v_cmp_lt_i32_e32 vcc, v1, v15
	v_max_f32_e32 v8, v9, v8
	v_dot2c_f32_f16_e32 v3, v97, v97
	v_cndmask_b32_e32 v1, v14, v1, vcc
	v_max3_f32 v8, v10, v11, v8
	v_dot2c_f32_f16_e32 v3, v90, v90
	v_lshlrev_b32_e32 v1, 2, v1
	v_max3_f32 v6, v6, v7, v8
	v_dot2c_f32_f16_e32 v3, v91, v91
	ds_bpermute_b32 v7, v1, v6
	v_dot2c_f32_f16_e32 v3, v92, v92
	v_dot2c_f32_f16_e32 v3, v93, v93
	v_dot2c_f32_f16_e32 v3, v86, v86
	v_dot2c_f32_f16_e32 v3, v87, v87
	v_dot2c_f32_f16_e32 v3, v88, v88
	s_waitcnt lgkmcnt(0)
	v_max_f32_e32 v7, v7, v7
	v_dot2c_f32_f16_e32 v3, v89, v89
	v_max_f32_e32 v6, v6, v7
	v_xor_b32_e32 v7, 16, v14
	v_dot2c_f32_f16_e32 v3, v82, v82
	v_cmp_lt_i32_e32 vcc, v7, v15
	v_dot2c_f32_f16_e32 v3, v83, v83
	v_dot2c_f32_f16_e32 v3, v84, v84
	v_cndmask_b32_e32 v7, v14, v7, vcc
	v_lshlrev_b32_e32 v165, 2, v7
	v_dot2c_f32_f16_e32 v3, v85, v85
	ds_bpermute_b32 v7, v165, v6
	v_dot2c_f32_f16_e32 v3, v78, v78
	v_dot2c_f32_f16_e32 v3, v79, v79
	v_dot2c_f32_f16_e32 v3, v80, v80
	v_dot2c_f32_f16_e32 v3, v81, v81
	v_dot2c_f32_f16_e32 v3, v74, v74
	s_waitcnt lgkmcnt(0)
	v_max_f32_e32 v7, v7, v7
	v_dot2c_f32_f16_e32 v3, v75, v75
	v_max_f32_e32 v6, v6, v7
	v_xor_b32_e32 v7, 8, v14
	v_dot2c_f32_f16_e32 v3, v76, v76
	v_cmp_lt_i32_e32 vcc, v7, v15
	v_dot2c_f32_f16_e32 v3, v77, v77
	v_dot2c_f32_f16_e32 v3, v70, v70
	v_cndmask_b32_e32 v7, v14, v7, vcc
	v_lshlrev_b32_e32 v172, 2, v7
	v_dot2c_f32_f16_e32 v3, v71, v71
	ds_bpermute_b32 v7, v172, v6
	v_dot2c_f32_f16_e32 v3, v72, v72
	v_dot2c_f32_f16_e32 v3, v73, v73
	v_dot2c_f32_f16_e32 v3, v66, v66
	v_dot2c_f32_f16_e32 v3, v67, v67
	v_dot2c_f32_f16_e32 v3, v68, v68
	s_waitcnt lgkmcnt(0)
	v_max_f32_e32 v7, v7, v7
	v_dot2c_f32_f16_e32 v3, v69, v69
	v_max_f32_e32 v6, v6, v7
	v_xor_b32_e32 v7, 4, v14
	v_dot2c_f32_f16_e32 v3, v62, v62
	v_cmp_lt_i32_e32 vcc, v7, v15
	v_dot2c_f32_f16_e32 v3, v63, v63
	v_dot2c_f32_f16_e32 v3, v64, v64
	v_cndmask_b32_e32 v7, v14, v7, vcc
	v_lshlrev_b32_e32 v173, 2, v7
	v_dot2c_f32_f16_e32 v3, v65, v65
	ds_bpermute_b32 v7, v173, v6
	v_dot2c_f32_f16_e32 v3, v58, v58
	v_dot2c_f32_f16_e32 v3, v59, v59
	v_dot2c_f32_f16_e32 v3, v60, v60
	v_dot2c_f32_f16_e32 v3, v61, v61
	v_dot2c_f32_f16_e32 v3, v54, v54
	s_waitcnt lgkmcnt(0)
	v_max_f32_e32 v7, v7, v7
	v_dot2c_f32_f16_e32 v3, v55, v55
	v_max_f32_e32 v6, v6, v7
	v_xor_b32_e32 v7, 2, v14
	v_dot2c_f32_f16_e32 v3, v56, v56
	v_cmp_lt_i32_e32 vcc, v7, v15
	v_dot2c_f32_f16_e32 v3, v57, v57
	v_dot2c_f32_f16_e32 v3, v50, v50
	v_cndmask_b32_e32 v7, v14, v7, vcc
	v_lshlrev_b32_e32 v174, 2, v7
	v_dot2c_f32_f16_e32 v3, v51, v51
	ds_bpermute_b32 v7, v174, v6
	v_dot2c_f32_f16_e32 v3, v52, v52
	v_dot2c_f32_f16_e32 v3, v53, v53
	v_dot2c_f32_f16_e32 v3, v46, v46
	v_dot2c_f32_f16_e32 v3, v47, v47
	v_dot2c_f32_f16_e32 v3, v48, v48
	s_waitcnt lgkmcnt(0)
	v_max_f32_e32 v7, v7, v7
	v_dot2c_f32_f16_e32 v3, v49, v49
	v_max_f32_e32 v6, v6, v7
	v_xor_b32_e32 v7, 1, v14
	v_dot2c_f32_f16_e32 v3, v42, v42
	v_cmp_lt_i32_e32 vcc, v7, v15
	v_dot2c_f32_f16_e32 v3, v43, v43
	v_dot2c_f32_f16_e32 v3, v44, v44
	v_cndmask_b32_e32 v7, v14, v7, vcc
	v_lshlrev_b32_e32 v175, 2, v7
	v_dot2c_f32_f16_e32 v3, v45, v45
	ds_bpermute_b32 v7, v175, v6
	v_dot2c_f32_f16_e32 v3, v38, v38
	v_dot2c_f32_f16_e32 v3, v39, v39
	v_dot2c_f32_f16_e32 v3, v40, v40
	v_dot2c_f32_f16_e32 v3, v41, v41
	v_dot2c_f32_f16_e32 v3, v34, v34
	s_waitcnt lgkmcnt(0)
	v_max_f32_e32 v7, v7, v7
	v_dot2c_f32_f16_e32 v3, v35, v35
	v_max_f32_e32 v6, v6, v7
	v_dot2c_f32_f16_e32 v3, v36, v36
	v_add_f32_e32 v6, v6, v6
	s_mov_b32 s41, 0xf800000
	v_dot2c_f32_f16_e32 v3, v37, v37
	v_mul_f32_e32 v7, 0x4f800000, v6
	v_cmp_gt_f32_e32 vcc, s41, v6
	s_lshl_b32 s43, s33, 7
	ds_bpermute_b32 v8, v1, v3
	v_cndmask_b32_e32 v6, v6, v7, vcc
	v_sqrt_f32_e32 v7, v6
	s_lshl_b32 s36, s33, 2
	s_lshl_b32 s45, s33, 3
	s_waitcnt lgkmcnt(0)
	v_add_f32_e32 v178, v3, v8
	v_add_u32_e32 v3, -1, v7
	v_fma_f32 v8, -v3, v7, v6
	v_cmp_ge_f32_e64 s[4:5], 0, v8
	v_add_u32_e32 v8, 1, v7
	s_add_i32 s44, s36, 0x22620
	v_cndmask_b32_e64 v3, v7, v3, s[4:5]
	v_fma_f32 v7, -v8, v7, v6
	v_cmp_lt_f32_e64 s[4:5], 0, v7
	s_add_i32 s45, s45, 0x22600
	s_add_i32 s3, s43, 0x22000
	v_cndmask_b32_e64 v3, v3, v8, s[4:5]
	v_mul_f32_e32 v7, 0x37800000, v3
	s_add_i32 s46, s98, 0x18000
	s_add_i32 s47, s36, 0x21800
	s_add_i32 s48, s36, 0x21000
	v_cndmask_b32_e32 v3, v3, v7, vcc
	v_cmp_class_f32_e32 vcc, v6, v179
	s_add_u32 s10, s14, s10
	s_addc_u32 s11, s15, s11
	v_cndmask_b32_e32 v180, v3, v6, vcc
	v_mov_b32_e32 v3, 0x22200
	v_lshl_or_b32 v183, v4, 2, v3
	v_or_b32_e32 v188, 0x20800, v2
	v_lshl_add_u64 v[2:3], s[10:11], 0, v[162:163]
	s_mov_b64 s[10:11], 0x1c00
	s_mov_b32 s24, 0x39666666
	s_mov_b32 s40, 0
	s_mov_b32 s42, 0xff800000
	v_cmp_lt_u32_e64 s[12:13], 31, v164
	v_cmp_gt_u32_e64 s[4:5], 32, v164
	v_cmp_eq_u32_e64 s[8:9], 0, v0
	v_lshl_add_u32 v186, v164, 2, s3
	v_lshl_add_u64 v[168:169], v[2:3], 0, s[10:11]
	s_mov_b32 s25, 0x39800000
	s_mov_b32 s49, 0x7149f2ca
	s_mov_b64 s[26:27], 0x2000
	s_mov_b32 s3, 0
	s_mov_b32 s22, 0
	s_mov_b32 s37, 0
	s_mov_b32 s38, 0
	s_mov_b32 s39, 0
	s_mov_b32 s23, 0
	s_barrier
	s_branch .LBB1_6
